# v17 + P2 background conversion rebalanced between the 10-unit and the 9-unit workgroups: common share 13*2048 items (was 15*2048 / all for the early-slot groups), remainder to the 9-unit workgroups
# baseline (speedup 1.0000x reference)
.LBB0_219:
	s_cmp_lt_i32 s42, s33
	s_cselect_b64 s[14:15], -1, 0
	s_cmp_ge_i32 s42, s33
	s_cselect_b64 s[8:9], -1, 0
	s_add_u32 s40, s50, 0xd200000
	s_addc_u32 s41, s51, 0
	s_and_b64 vcc, exec, s[8:9]
	s_cbranch_vccnz .LBB0_330
	s_lshl_b32 s0, s86, 3
	s_add_i32 s63, s0, s88
	s_cmp_gt_i32 s63, 0x67ff
	s_waitcnt vmcnt(0)
	s_barrier
	s_cbranch_scc1 .LBB0_329
	s_ashr_i32 s0, s63, 9
	s_mulk_i32 s0, 0x300
	s_and_b32 s22, s63, 0x1ff
	s_add_i32 s23, s0, s22
	s_addk_i32 s23, 0x3000
	s_cmpk_gt_i32 s23, 0x25ff
	s_cbranch_scc0 .LBB0_228
	s_cmpk_gt_u32 s23, 0x27ff
	s_cbranch_scc0 .LBB0_229
	s_cmpk_gt_u32 s23, 0x2bff
	s_cbranch_scc0 .LBB0_230
	s_cmpk_gt_u32 s23, 0x2fff
	s_cbranch_scc0 .LBB0_231
	s_add_i32 s24, s23, 0xffffd000
	s_and_b32 s0, s24, 0xffff
	s_mul_i32 s0, s0, 0xaaab
	s_lshr_b32 s20, s0, 25
	s_mul_i32 s0, s20, 0x300
	s_sub_i32 s0, s24, s0
	s_and_b32 s21, s0, 0xffff
	s_cmpk_gt_u32 s21, 0x1ff
	s_cbranch_scc0 .LBB0_232
	s_cmpk_gt_u32 s24, 0xbfff
	s_cbranch_scc0 .LBB0_233
	s_add_i32 s0, 0, 0x27ea8
	v_mov_b32_e32 v2, s0
	ds_read_b64 v[2:3], v2
	s_mov_b64 s[16:17], 0
	s_waitcnt lgkmcnt(0)
	v_readfirstlane_b32 s0, v2
	v_readfirstlane_b32 s1, v3
	s_branch .LBB0_234

.LBB0_258:
	s_waitcnt lgkmcnt(0)
	s_add_i32 s63, s64, s27
	s_cmp_gt_i32 s63, 0x67ff
	s_cselect_b64 s[18:19], -1, 0

.LBB0_260:
	s_add_i32 s64, s63, s27
	s_cmp_lt_i32 s64, 0x6800
	s_cselect_b64 s[18:19], -1, 0
	s_cmp_gt_i32 s64, 0x67ff
	s_cbranch_scc1 .Lcva_d1
	s_ashr_i32 s16, s64, 9
	s_mulk_i32 s16, 0x300
	s_and_b32 s67, s64, 0x1ff
	s_add_i32 s68, s16, s67
	s_addk_i32 s68, 0x3000
	s_cmpk_gt_i32 s68, 0x25ff
	s_mov_b64 s[24:25], -1
	s_cbranch_scc0 .LBB0_286
	s_cmpk_gt_u32 s68, 0x27ff
	s_cbranch_scc0 .LBB0_283
	s_cmpk_gt_u32 s68, 0x2bff
	s_cbranch_scc0 .LBB0_280
	s_cmpk_gt_u32 s68, 0x2fff
	s_cbranch_scc0 .LBB0_277
	s_add_i32 s65, s68, 0xffffd000
	s_and_b32 s16, s65, 0xffff
	s_mul_i32 s16, s16, 0xaaab
	s_lshr_b32 s24, s16, 25
	s_mul_i32 s16, s24, 0x300
	s_sub_i32 s16, s65, s16
	s_and_b32 s25, s16, 0xffff
	s_cmpk_gt_u32 s25, 0x1ff
	s_mov_b64 s[22:23], -1
	s_cbranch_scc0 .LBB0_271
	s_cmpk_gt_u32 s65, 0xbfff
	s_mov_b64 s[20:21], -1
	s_cbranch_scc0 .LBB0_268
	v_mov_b32_e32 v58, s54
	ds_read_b64 v[58:59], v58
	s_mov_b64 s[20:21], 0
	s_waitcnt lgkmcnt(0)
	v_readfirstlane_b32 s16, v58
	v_readfirstlane_b32 s17, v59

.LBB0_292:
	s_waitcnt lgkmcnt(0)
	s_andn2_b64 vcc, exec, s[18:19]
	s_mov_b64 s[18:19], -1
	s_cbranch_vccnz .LBB0_259
	s_add_i32 s67, s53, s63
	s_cmp_gt_i32 s67, 0x67ff
	s_cbranch_scc1 .Lcva_d2
	s_ashr_i32 s0, s67, 9
	s_mulk_i32 s0, 0x300
	s_and_b32 s24, s67, 0x1ff
	s_add_i32 s25, s0, s24
	s_addk_i32 s25, 0x3000
	s_cmpk_gt_i32 s25, 0x25ff
	s_mov_b64 s[22:23], -1
	s_cbranch_scc0 .LBB0_323
	s_cmpk_gt_u32 s25, 0x27ff
	s_cbranch_scc0 .LBB0_320
	s_cmpk_gt_u32 s25, 0x2bff
	s_cbranch_scc0 .LBB0_317
	s_cmpk_gt_u32 s25, 0x2fff
	s_cbranch_scc0 .LBB0_314
	s_add_i32 s26, s25, 0xffffd000
	s_and_b32 s0, s26, 0xffff
	s_mul_i32 s0, s0, 0xaaab
	s_lshr_b32 s22, s0, 25
	s_mul_i32 s0, s22, 0x300
	s_sub_i32 s0, s26, s0
	s_and_b32 s23, s0, 0xffff
	s_cmpk_gt_u32 s23, 0x1ff
	s_mov_b64 s[20:21], -1
	s_cbranch_scc0 .LBB0_304
	s_cmpk_gt_u32 s26, 0xbfff
	s_mov_b64 s[18:19], -1
	s_cbranch_scc0 .LBB0_301
	v_mov_b32_e32 v2, s54
	ds_read_b64 v[2:3], v2
	s_mov_b64 s[18:19], 0
	s_waitcnt lgkmcnt(0)
	v_readfirstlane_b32 s0, v2
	v_readfirstlane_b32 s1, v3

.LBB0_376:
	s_andn2_b64 vcc, exec, s[8:9]
	s_cbranch_vccnz .LBB0_599
	s_cmpk_eq_i32 s52, 0x100
	s_cselect_b64 s[0:1], -1, 0
	s_movk_i32 s10, 0x6800
	s_and_b64 s[8:9], s[0:1], exec
	s_cselect_b32 s21, s10, 0x8200
	s_lshl_b32 s8, s86, 3
	s_add_i32 s57, s8, s88
	s_mul_i32 s8, s88, 0x4100
	s_add_i32 s20, s8, 0
	s_cmp_ge_i32 s57, s21
	s_waitcnt vmcnt(0)
	s_barrier
	s_cbranch_scc1 .LBB0_486
	s_ashr_i32 s8, s57, 9
	s_mulk_i32 s8, 0x300
	s_and_b32 s16, s57, 0x1ff
	s_add_i32 s17, s8, s16
	s_addk_i32 s17, 0x3000
	s_cmpk_gt_i32 s17, 0x25ff
	s_cbranch_scc0 .LBB0_385
	s_cmpk_gt_u32 s17, 0x27ff
	s_cbranch_scc0 .LBB0_386
	s_cmpk_gt_u32 s17, 0x2bff
	s_cbranch_scc0 .LBB0_387
	s_cmpk_gt_u32 s17, 0x2fff
	s_cbranch_scc0 .LBB0_388
	s_add_i32 s18, s17, 0xffffd000
	s_and_b32 s8, s18, 0xffff
	s_mul_i32 s8, s8, 0xaaab
	s_lshr_b32 s14, s8, 25
	s_mul_i32 s8, s14, 0x300
	s_sub_i32 s8, s18, s8
	s_and_b32 s15, s8, 0xffff
	s_cmpk_gt_u32 s15, 0x1ff
	s_cbranch_scc0 .LBB0_389
	s_cmpk_gt_u32 s18, 0xbfff
	s_cbranch_scc0 .LBB0_390
	s_add_i32 s8, 0, 0x27ea8
	v_mov_b32_e32 v2, s8
	ds_read_b64 v[2:3], v2
	s_mov_b64 s[10:11], 0
	s_waitcnt lgkmcnt(0)
	v_readfirstlane_b32 s8, v2
	v_readfirstlane_b32 s9, v3
	s_branch .LBB0_391

.LBB0_486:
	s_cmpk_lt_i32 s90, 0x80
	s_cselect_b64 s[8:9], -1, 0
	s_xor_b64 s[0:1], s[0:1], -1
	s_or_b64 s[0:1], s[8:9], s[0:1]
	s_and_b64 vcc, exec, s[0:1]
	s_cbranch_vccnz .LBB0_598
	s_lshl_b32 s14, s90, 3
	s_add_i32 s14, s14, s88
	s_add_i32 s17, s14, 0xfffffc00
	s_cmpk_gt_i32 s17, 0x19ff
	s_cbranch_scc1 .LBB0_598
	s_add_i32 s0, s17, 0x6800
	s_ashr_i32 s0, s0, 9
	s_and_b32 s15, s17, 0x1ff
	s_mul_i32 s16, s0, 0x300
	s_or_b32 s18, s15, 0x3000
	s_add_i32 s16, s16, s18
	s_cmpk_gt_i32 s16, 0x25ff
	s_cbranch_scc0 .LBB0_495
	s_cmpk_gt_u32 s16, 0x27ff
	s_cbranch_scc0 .LBB0_496
	s_cmpk_gt_u32 s16, 0x2bff
	s_cbranch_scc0 .LBB0_497
	s_cmpk_gt_u32 s16, 0x2fff
	s_cbranch_scc0 .LBB0_498
	s_add_i32 s19, s16, 0xffffd000
	s_and_b32 s0, s19, 0xffff
	s_mul_i32 s0, s0, 0xaaab
	s_lshr_b32 s12, s0, 25
	s_mul_i32 s0, s12, 0x300
	s_sub_i32 s0, s19, s0
	s_and_b32 s13, s0, 0xffff
	s_cmpk_gt_u32 s13, 0x1ff
	s_cbranch_scc0 .LBB0_499
	s_cmpk_gt_u32 s19, 0xbfff
	s_cbranch_scc0 .LBB0_500
	s_add_i32 s0, 0, 0x27ea8
	s_waitcnt vmcnt(15)
	v_mov_b32_e32 v2, s0
	ds_read_b64 v[2:3], v2
	s_mov_b64 s[8:9], 0
	s_waitcnt lgkmcnt(0)
	v_readfirstlane_b32 s0, v2
	v_readfirstlane_b32 s1, v3
	s_branch .LBB0_501

.LBB0_524:
	v_lshrrev_b32_e32 v131, 4, v196
	s_waitcnt vmcnt(15)
	v_mul_u32_u24_e32 v2, s10, v131
	v_and_b32_e32 v130, 60, v204
	v_mov_b32_e32 v133, 0
	s_waitcnt lgkmcnt(0)
	v_lshlrev_b32_e32 v132, 2, v2
	v_lshl_add_u64 v[2:3], s[8:9], 0, v[132:133]
	v_lshlrev_b32_e32 v132, 2, v130
	v_or_b32_e32 v135, 4, v131
	s_waitcnt vmcnt(13)
	v_lshl_add_u64 v[10:11], v[2:3], 0, v[132:133]
	v_mul_u32_u24_e32 v2, s10, v135
	v_lshlrev_b32_e32 v2, 2, v2
	v_mov_b32_e32 v3, v133
	v_lshl_add_u64 v[2:3], s[8:9], 0, v[2:3]
	v_or_b32_e32 v139, 8, v131
	v_lshl_add_u64 v[12:13], v[2:3], 0, v[132:133]
	global_load_dwordx4 v[2:5], v[10:11], off nt
	global_load_dwordx4 v[6:9], v[12:13], off nt
	v_mul_u32_u24_e32 v10, s10, v139
	v_lshlrev_b32_e32 v10, 2, v10
	v_mov_b32_e32 v11, v133
	v_lshl_add_u64 v[10:11], s[8:9], 0, v[10:11]
	v_or_b32_e32 v141, 12, v131
	s_waitcnt vmcnt(13)
	v_lshl_add_u64 v[18:19], v[10:11], 0, v[132:133]
	v_mul_u32_u24_e32 v10, s10, v141
	v_lshlrev_b32_e32 v10, 2, v10
	v_mov_b32_e32 v11, v133
	v_lshl_add_u64 v[10:11], s[8:9], 0, v[10:11]
	v_or_b32_e32 v143, 16, v131
	v_lshl_add_u64 v[20:21], v[10:11], 0, v[132:133]
	global_load_dwordx4 v[10:13], v[18:19], off nt
	global_load_dwordx4 v[14:17], v[20:21], off nt
	v_mul_u32_u24_e32 v18, s10, v143
	v_lshlrev_b32_e32 v18, 2, v18
	v_mov_b32_e32 v19, v133
	v_lshl_add_u64 v[18:19], s[8:9], 0, v[18:19]
	v_or_b32_e32 v145, 20, v131
	s_waitcnt vmcnt(13)
	v_lshl_add_u64 v[26:27], v[18:19], 0, v[132:133]
	v_mul_u32_u24_e32 v18, s10, v145
	v_lshlrev_b32_e32 v18, 2, v18
	v_mov_b32_e32 v19, v133
	v_lshl_add_u64 v[18:19], s[8:9], 0, v[18:19]
	v_or_b32_e32 v147, 24, v131
	v_lshl_add_u64 v[28:29], v[18:19], 0, v[132:133]
	global_load_dwordx4 v[18:21], v[26:27], off nt
	global_load_dwordx4 v[22:25], v[28:29], off nt
	v_mul_u32_u24_e32 v26, s10, v147
	v_lshlrev_b32_e32 v26, 2, v26
	v_mov_b32_e32 v27, v133
	v_lshl_add_u64 v[26:27], s[8:9], 0, v[26:27]
	v_or_b32_e32 v149, 28, v131
	s_waitcnt vmcnt(13)
	v_lshl_add_u64 v[34:35], v[26:27], 0, v[132:133]
	v_mul_u32_u24_e32 v26, s10, v149
	v_lshlrev_b32_e32 v26, 2, v26
	v_mov_b32_e32 v27, v133
	v_lshl_add_u64 v[26:27], s[8:9], 0, v[26:27]
	v_or_b32_e32 v151, 32, v131
	v_lshl_add_u64 v[36:37], v[26:27], 0, v[132:133]
	global_load_dwordx4 v[26:29], v[34:35], off nt
	global_load_dwordx4 v[30:33], v[36:37], off nt
	v_mul_u32_u24_e32 v34, s10, v151
	v_lshlrev_b32_e32 v34, 2, v34
	v_mov_b32_e32 v35, v133
	v_lshl_add_u64 v[34:35], s[8:9], 0, v[34:35]
	v_or_b32_e32 v163, 36, v131
	s_waitcnt vmcnt(13)
	v_lshl_add_u64 v[42:43], v[34:35], 0, v[132:133]
	v_mul_u32_u24_e32 v34, s10, v163
	v_lshlrev_b32_e32 v34, 2, v34
	v_mov_b32_e32 v35, v133
	v_lshl_add_u64 v[34:35], s[8:9], 0, v[34:35]
	v_or_b32_e32 v165, 40, v131
	v_lshl_add_u64 v[44:45], v[34:35], 0, v[132:133]
	global_load_dwordx4 v[34:37], v[42:43], off nt
	global_load_dwordx4 v[38:41], v[44:45], off nt
	v_mul_u32_u24_e32 v42, s10, v165
	v_lshlrev_b32_e32 v42, 2, v42
	v_mov_b32_e32 v43, v133
	v_lshl_add_u64 v[42:43], s[8:9], 0, v[42:43]
	v_or_b32_e32 v167, 44, v131
	s_waitcnt vmcnt(13)
	v_lshl_add_u64 v[50:51], v[42:43], 0, v[132:133]
	v_mul_u32_u24_e32 v42, s10, v167
	v_lshlrev_b32_e32 v42, 2, v42
	v_mov_b32_e32 v43, v133
	v_lshl_add_u64 v[42:43], s[8:9], 0, v[42:43]
	v_or_b32_e32 v169, 48, v131
	v_lshl_add_u64 v[52:53], v[42:43], 0, v[132:133]
	global_load_dwordx4 v[42:45], v[50:51], off nt
	global_load_dwordx4 v[46:49], v[52:53], off nt
	v_mul_u32_u24_e32 v50, s10, v169
	v_lshlrev_b32_e32 v50, 2, v50
	v_mov_b32_e32 v51, v133
	v_lshl_add_u64 v[50:51], s[8:9], 0, v[50:51]
	v_or_b32_e32 v171, 52, v131
	v_lshl_add_u64 v[58:59], v[50:51], 0, v[132:133]
	v_mul_u32_u24_e32 v50, s10, v171
	v_lshlrev_b32_e32 v50, 2, v50
	v_mov_b32_e32 v51, v133
	v_lshl_add_u64 v[50:51], s[8:9], 0, v[50:51]
	v_or_b32_e32 v180, 56, v131
	v_lshl_add_u64 v[60:61], v[50:51], 0, v[132:133]
	global_load_dwordx4 v[50:53], v[58:59], off nt
	global_load_dwordx4 v[54:57], v[60:61], off nt
	v_mul_u32_u24_e32 v58, s10, v180
	v_or_b32_e32 v181, 60, v131
	v_lshlrev_b32_e32 v58, 2, v58
	v_mov_b32_e32 v59, v133
	v_mul_u32_u24_e32 v60, s10, v181
	v_lshl_add_u64 v[58:59], s[8:9], 0, v[58:59]
	v_lshlrev_b32_e32 v60, 2, v60
	v_mov_b32_e32 v61, v133
	v_lshl_add_u64 v[58:59], v[58:59], 0, v[132:133]
	v_lshl_add_u64 v[60:61], s[8:9], 0, v[60:61]
	v_lshl_add_u64 v[60:61], v[60:61], 0, v[132:133]
	global_load_dwordx4 v[74:77], v[58:59], off nt
	global_load_dwordx4 v[78:81], v[60:61], off nt
	s_lshl_b32 s8, s15, 5
	s_and_b32 s22, s8, 0xc0
	s_lshl_b32 s8, s15, 6
	s_bfe_u32 s21, s87, 0x10006
	s_and_b32 s23, s8, 64
	s_add_u32 s25, s50, 0x14400000
	s_addc_u32 s26, s51, 0
	s_add_u32 s27, s50, 0x4000000
	s_addc_u32 s28, s51, 0
	s_add_u32 s29, s50, 0x1600000
	s_addc_u32 s30, s51, 0
	s_add_u32 s31, s50, 0xe00000
	s_addc_u32 s33, s51, 0
	v_and_b32_e32 v60, 7, v0
	v_lshrrev_b32_e32 v134, 3, v196
	v_add_u32_e32 v58, s20, v132
	v_mul_u32_u24_e32 v59, 0x104, v131
	s_add_u32 s34, s50, 0xa00000
	v_mul_u32_u24_e32 v61, 0x820, v60
	v_lshlrev_b32_e32 v62, 2, v134
	s_addc_u32 s35, s51, 0
	v_lshlrev_b32_e32 v136, 3, v60
	v_mov_b32_e32 v137, v133
	v_add3_u32 v182, s20, v61, v62
	v_or_b32_e32 v138, 8, v134
	v_or_b32_e32 v140, 16, v134
	v_or_b32_e32 v142, 24, v134
	v_or_b32_e32 v144, 32, v134
	v_or_b32_e32 v146, 40, v134
	v_or_b32_e32 v148, 48, v134
	v_or_b32_e32 v150, 56, v134
	v_lshlrev_b32_e32 v152, 4, v60
	v_mov_b32_e32 v153, v133
	s_add_i32 s57, s14, 0x5c00
	s_add_i32 s20, 0, 0x27ea8
	s_add_i32 s37, 0, 0x27e90
	s_movk_i32 s42, 0x98
	s_movk_i32 s43, 0x88
	s_add_i32 s44, 0, 0x27e60
	s_add_i32 s45, 0, 0x27e58
	s_add_i32 s46, 0, 0x27e50
	s_add_i32 s47, 0, 0x27e30
	s_mov_b32 s53, 0xc3e00000
	v_add_u32_e32 v183, v58, v59
	v_mov_b32_e32 v184, 0x43e00000
	s_mov_b32 s56, s24
	s_mov_b32 s55, s19
	s_mov_b64 s[8:9], s[0:1]
	s_branch .LBB0_528
